# next-row cache-warming loads also in the dense and MoE N2 norm row loops (plus N1)
# baseline (speedup 1.0000x reference)
.LBB0_1217:
	v_lshl_add_u64 v[242:243], v[198:199], 0, v[200:201]
	global_load_dwordx2 v[184:185], v[198:199], off offset:-1024
	global_load_dwordx2 v[186:187], v[198:199], off offset:-512
	global_load_dwordx2 v[206:207], v[198:199], off
	global_load_dwordx2 v[208:209], v[198:199], off offset:512
	global_load_dwordx2 v[244:245], v[242:243], off offset:-1024
	global_load_dwordx2 v[244:245], v[242:243], off offset:-512
	global_load_dwordx2 v[244:245], v[242:243], off
	global_load_dwordx2 v[244:245], v[242:243], off offset:512
	s_mov_b32 s0, 0xf800000
	s_mov_b32 s10, 0x42fe0000
	s_waitcnt vmcnt(6) lgkmcnt(3)
	v_and_b32_e32 v215, 0xffff0000, v187
	v_and_b32_e32 v214, 0xffff0000, v186
	s_waitcnt vmcnt(4) lgkmcnt(0)
	v_lshlrev_b32_e32 v221, 16, v208
	v_and_b32_e32 v219, 0xffff0000, v208
	v_lshlrev_b32_e32 v222, 16, v209
	v_and_b32_e32 v223, 0xffff0000, v209
	v_lshlrev_b32_e32 v208, 16, v184
	v_and_b32_e32 v209, 0xffff0000, v184
	v_lshlrev_b32_e32 v184, 16, v185
	v_and_b32_e32 v185, 0xffff0000, v185
	v_mul_f32_e32 v210, v185, v185
	v_pk_fma_f32 v[228:229], v[184:185], v[184:185], v[210:211] op_sel_hi:[1,1,0]
	v_lshlrev_b32_e32 v210, 16, v206
	v_and_b32_e32 v211, 0xffff0000, v206
	v_mul_f32_e32 v206, v209, v209
	v_lshlrev_b32_e32 v213, 16, v187
	v_lshlrev_b32_e32 v212, 16, v186
	v_pk_mul_f32 v[186:187], v[214:215], v[214:215]
	v_lshlrev_b32_e32 v216, 16, v207
	v_and_b32_e32 v217, 0xffff0000, v207
	v_pk_fma_f32 v[206:207], v[208:209], v[208:209], v[206:207] op_sel_hi:[1,1,0]
	v_pk_fma_f32 v[186:187], v[212:213], v[212:213], v[186:187]
	v_mov_b32_e32 v220, v206
	v_mov_b32_e32 v230, v228
	v_mov_b32_e32 v231, v221
	v_mul_f32_e32 v218, v219, v219
	v_pk_add_f32 v[206:207], v[206:207], v[228:229]
	v_pk_mul_f32 v[228:229], v[220:221], v[230:231]
	v_pk_add_f32 v[186:187], v[186:187], v[186:187] op_sel:[0,1] op_sel_hi:[1,0]
	v_mov_b32_e32 v207, v229
	v_mov_b32_e32 v187, v218
	v_pk_add_f32 v[186:187], v[206:207], v[186:187]
	v_mul_f32_e32 v206, v211, v211
	v_mul_f32_e32 v218, v217, v217
	v_mul_f32_e32 v227, v222, v222
	v_mul_f32_e32 v232, v223, v223
	v_pk_fma_f32 v[206:207], v[210:211], v[210:211], v[206:207] op_sel_hi:[1,1,0]
	v_pk_fma_f32 v[228:229], v[216:217], v[216:217], v[218:219] op_sel_hi:[1,1,0]
	v_mov_b32_e32 v207, v227
	v_mov_b32_e32 v229, v232
	v_pk_add_f32 v[206:207], v[206:207], v[228:229]
	s_nop 0
	v_pk_add_f32 v[186:187], v[186:187], v[206:207]
	s_nop 0
	v_add_f32_e32 v186, v186, v187
	ds_bpermute_b32 v187, v1, v186
	s_waitcnt lgkmcnt(0)
	v_add_f32_e32 v186, v186, v187
	ds_bpermute_b32 v187, v181, v186
	s_waitcnt lgkmcnt(0)
	v_add_f32_e32 v186, v186, v187
	ds_bpermute_b32 v187, v183, v186
	s_waitcnt lgkmcnt(0)
	v_add_f32_e32 v186, v186, v187
	ds_bpermute_b32 v187, v224, v186
	s_waitcnt lgkmcnt(0)
	v_add_f32_e32 v186, v186, v187
	ds_bpermute_b32 v187, v225, v186
	s_waitcnt lgkmcnt(0)
	v_add_f32_e32 v186, v186, v187
	ds_bpermute_b32 v187, v226, v186
	s_waitcnt lgkmcnt(0)
	v_add_f32_e32 v186, v186, v187
	v_fmamk_f32 v186, v186, 0x3a800000, v241
	v_cmp_gt_f32_e32 vcc, s0, v186
	v_mul_f32_e32 v187, 0x4f800000, v186
	s_nop 0
	v_cndmask_b32_e32 v186, v186, v187, vcc
	v_sqrt_f32_e32 v187, v186
	s_nop 0
	v_add_u32_e32 v206, -1, v187
	v_fma_f32 v207, -v206, v187, v186
	v_cmp_ge_f32_e64 s[0:1], 0, v207
	v_add_u32_e32 v207, 1, v187
	s_nop 0
	v_cndmask_b32_e64 v206, v187, v206, s[0:1]
	v_fma_f32 v187, -v207, v187, v186
	v_cmp_lt_f32_e64 s[0:1], 0, v187
	s_nop 1
	v_cndmask_b32_e64 v187, v206, v207, s[0:1]
	v_mul_f32_e32 v206, 0x37800000, v187
	v_cndmask_b32_e32 v187, v187, v206, vcc
	v_cmp_class_f32_e32 vcc, v186, v188
	s_nop 1
	v_cndmask_b32_e32 v186, v187, v186, vcc
	v_div_scale_f32 v187, s[0:1], v186, v186, 1.0
	v_rcp_f32_e32 v206, v187
	s_nop 0
	v_fma_f32 v207, -v187, v206, 1.0
	v_fmac_f32_e32 v206, v207, v206
	v_div_scale_f32 v207, vcc, 1.0, v186, 1.0
	v_mul_f32_e32 v218, v207, v206
	v_fma_f32 v220, -v187, v218, v207
	v_fmac_f32_e32 v218, v220, v206
	v_fma_f32 v187, -v187, v218, v207
	v_div_fmas_f32 v187, v187, v206, v218
	v_div_fixup_f32 v220, v187, v186, 1.0
	v_pk_mul_f32 v[184:185], v[220:221], v[184:185] op_sel_hi:[0,1]
	v_pk_mul_f32 v[184:185], v[4:5], v[184:185]
	v_pk_add_f32 v[206:207], v[150:151], 1.0 op_sel_hi:[1,0]
	v_pk_mul_f32 v[186:187], v[220:221], v[208:209] op_sel_hi:[0,1]
	v_pk_fma_f32 v[206:207], v[206:207], v[184:185], v[162:163]
	v_mov_b32_e32 v184, v213
	v_mov_b32_e32 v185, v215
	v_pk_mul_f32 v[186:187], v[2:3], v[186:187]
	v_pk_add_f32 v[208:209], v[148:149], 1.0 op_sel_hi:[1,0]
	v_pk_mul_f32 v[184:185], v[220:221], v[184:185] op_sel_hi:[0,1]
	v_mov_b32_e32 v213, v214
	v_pk_fma_f32 v[208:209], v[208:209], v[186:187], v[160:161]
	v_pk_mul_f32 v[186:187], v[220:221], v[212:213] op_sel_hi:[0,1]
	v_pk_mul_f32 v[184:185], v[8:9], v[184:185]
	v_pk_add_f32 v[212:213], v[154:155], 1.0 op_sel_hi:[1,0]
	v_pk_mul_f32 v[186:187], v[6:7], v[186:187]
	v_pk_add_f32 v[214:215], v[152:153], 1.0 op_sel_hi:[1,0]
	v_pk_fma_f32 v[212:213], v[212:213], v[184:185], v[158:159]
	v_pk_mul_f32 v[184:185], v[220:221], v[216:217] op_sel_hi:[0,1]
	v_pk_fma_f32 v[214:215], v[214:215], v[186:187], v[156:157]
	v_pk_mul_f32 v[186:187], v[220:221], v[210:211] op_sel_hi:[0,1]
	v_pk_mul_f32 v[184:185], v[12:13], v[184:185]
	v_pk_add_f32 v[210:211], v[166:167], 1.0 op_sel_hi:[1,0]
	v_pk_mul_f32 v[186:187], v[10:11], v[186:187]
	v_pk_add_f32 v[216:217], v[164:165], 1.0 op_sel_hi:[1,0]
	v_pk_fma_f32 v[210:211], v[210:211], v[184:185], v[170:171]
	v_pk_mul_f32 v[184:185], v[222:223], v[220:221] op_sel_hi:[1,0]
	v_mov_b32_e32 v218, v221
	v_pk_fma_f32 v[216:217], v[216:217], v[186:187], v[168:169]
	v_pk_mul_f32 v[186:187], v[218:219], v[220:221] op_sel_hi:[1,0]
	v_pk_mul_f32 v[218:219], v[16:17], v[184:185]
	v_pk_add_f32 v[184:185], v[174:175], 1.0 op_sel_hi:[1,0]
	v_pk_mul_f32 v[220:221], v[14:15], v[186:187]
	v_pk_add_f32 v[186:187], v[172:173], 1.0 op_sel_hi:[1,0]
	v_pk_fma_f32 v[218:219], v[184:185], v[218:219], v[178:179]
	v_max_f32_e64 v184, |v208|, |v209|
	v_max_f32_e64 v185, |v206|, |v207|
	v_pk_fma_f32 v[220:221], v[186:187], v[220:221], v[176:177]
	v_max3_f32 v184, v184, 0, v185
	v_max_f32_e64 v185, |v214|, |v215|
	v_max_f32_e64 v186, |v212|, |v213|
	v_max3_f32 v184, v184, v185, v186
	v_max_f32_e64 v185, |v216|, |v217|
	v_max_f32_e64 v186, |v210|, |v211|
	v_max3_f32 v184, v184, v185, v186
	v_max_f32_e64 v185, |v220|, |v221|
	v_max_f32_e64 v186, |v218|, |v219|
	v_max3_f32 v184, v184, v185, v186
	ds_bpermute_b32 v185, v1, v184
	s_waitcnt lgkmcnt(0)
	v_max_f32_e32 v185, v185, v185
	v_max_f32_e32 v184, v184, v185
	ds_bpermute_b32 v185, v181, v184
	s_waitcnt lgkmcnt(0)
	v_max_f32_e32 v185, v185, v185
	v_max_f32_e32 v184, v184, v185
	ds_bpermute_b32 v185, v183, v184
	s_waitcnt lgkmcnt(0)
	v_max_f32_e32 v185, v185, v185
	v_max_f32_e32 v184, v184, v185
	ds_bpermute_b32 v185, v224, v184
	s_waitcnt lgkmcnt(0)
	v_max_f32_e32 v185, v185, v185
	v_max_f32_e32 v184, v184, v185
	ds_bpermute_b32 v185, v225, v184
	s_waitcnt lgkmcnt(0)
	v_max_f32_e32 v185, v185, v185
	v_max_f32_e32 v184, v184, v185
	ds_bpermute_b32 v185, v226, v184
	s_waitcnt lgkmcnt(0)
	v_max_f32_e32 v185, v185, v185
	v_max_f32_e32 v222, v184, v185
	v_div_scale_f32 v184, s[2:3], v222, v222, s10
	v_rcp_f32_e32 v185, v184
	v_cmp_lt_f32_e64 s[0:1], 0, v222
	v_fma_f32 v186, -v184, v185, 1.0
	v_fmac_f32_e32 v185, v186, v185
	v_div_scale_f32 v186, vcc, s10, v222, s10
	v_mul_f32_e32 v187, v186, v185
	v_fma_f32 v223, -v184, v187, v186
	v_fmac_f32_e32 v187, v223, v185
	v_fma_f32 v184, -v184, v187, v186
	v_div_fmas_f32 v184, v184, v185, v187
	v_div_fixup_f32 v184, v184, v222, s10
	v_cndmask_b32_e64 v184, 0, v184, s[0:1]
	v_mul_f32_e32 v186, v209, v184
	v_mul_f32_e32 v185, v208, v184
	v_rndne_f32_e32 v186, v186
	v_mul_f32_e32 v187, v206, v184
	v_mul_f32_e32 v223, v207, v184
	v_rndne_f32_e32 v185, v185
	v_cvt_i32_f32_e32 v186, v186
	v_rndne_f32_e32 v187, v187
	v_rndne_f32_e32 v223, v223
	v_cvt_i32_f32_e32 v185, v185
	v_cvt_i32_f32_sdwa v187, v187 dst_sel:WORD_1 dst_unused:UNUSED_PAD src0_sel:DWORD
	v_cvt_i32_f32_e32 v223, v223
	v_lshlrev_b32_e32 v186, 8, v186
	s_mov_b32 s0, 0x40c0c00
	v_and_b32_e32 v186, 0xff00, v186
	v_and_b32_e32 v187, 0xff0000, v187
	v_perm_b32 v185, v223, v185, s0
	v_or3_b32 v185, v185, v186, v187
	v_mul_f32_e32 v186, v215, v184
	global_store_dword v[194:195], v185, off offset:-512
	v_mul_f32_e32 v185, v214, v184
	v_rndne_f32_e32 v186, v186
	v_mul_f32_e32 v187, v212, v184
	v_mul_f32_e32 v223, v213, v184
	v_rndne_f32_e32 v185, v185
	v_cvt_i32_f32_e32 v186, v186
	v_rndne_f32_e32 v187, v187
	v_rndne_f32_e32 v223, v223
	v_cvt_i32_f32_e32 v185, v185
	v_cvt_i32_f32_sdwa v187, v187 dst_sel:WORD_1 dst_unused:UNUSED_PAD src0_sel:DWORD
	v_cvt_i32_f32_e32 v223, v223
	v_lshlrev_b32_e32 v186, 8, v186
	v_and_b32_e32 v186, 0xff00, v186
	v_and_b32_e32 v187, 0xff0000, v187
	v_perm_b32 v185, v223, v185, s0
	v_or3_b32 v185, v185, v186, v187
	v_mul_f32_e32 v186, v217, v184
	global_store_dword v[194:195], v185, off offset:-256
	v_mul_f32_e32 v185, v216, v184
	v_rndne_f32_e32 v186, v186
	v_mul_f32_e32 v187, v210, v184
	v_mul_f32_e32 v223, v211, v184
	v_rndne_f32_e32 v185, v185
	v_cvt_i32_f32_e32 v186, v186
	v_rndne_f32_e32 v187, v187
	v_rndne_f32_e32 v223, v223
	v_cvt_i32_f32_e32 v185, v185
	v_cvt_i32_f32_sdwa v187, v187 dst_sel:WORD_1 dst_unused:UNUSED_PAD src0_sel:DWORD
	v_cvt_i32_f32_e32 v223, v223
	v_lshlrev_b32_e32 v186, 8, v186
	v_and_b32_e32 v186, 0xff00, v186
	v_and_b32_e32 v187, 0xff0000, v187
	v_perm_b32 v185, v223, v185, s0
	v_or3_b32 v185, v185, v186, v187
	v_mul_f32_e32 v186, v221, v184
	global_store_dword v[194:195], v185, off
	v_mul_f32_e32 v185, v220, v184
	v_rndne_f32_e32 v186, v186
	v_mul_f32_e32 v187, v218, v184
	v_mul_f32_e32 v184, v219, v184
	v_rndne_f32_e32 v185, v185
	v_cvt_i32_f32_e32 v186, v186
	v_rndne_f32_e32 v187, v187
	v_rndne_f32_e32 v184, v184
	v_cvt_i32_f32_e32 v185, v185
	v_cvt_i32_f32_sdwa v187, v187 dst_sel:WORD_1 dst_unused:UNUSED_PAD src0_sel:DWORD
	v_cvt_i32_f32_e32 v184, v184
	v_lshlrev_b32_e32 v186, 8, v186
	v_and_b32_e32 v186, 0xff00, v186
	v_and_b32_e32 v187, 0xff0000, v187
	v_perm_b32 v184, v184, v185, s0
	v_or3_b32 v184, v184, v186, v187
	global_store_dword v[194:195], v184, off offset:256
	s_and_saveexec_b64 s[0:1], s[36:37]
	s_cbranch_execz .LBB0_1219
	v_mul_f32_e32 v184, 0x3c010204, v222
	global_store_dword v[204:205], v184, off

.LBB0_1630:
	v_readlane_b32 s40, v251, 5
	v_readlane_b32 s46, v251, 11
	v_readlane_b32 s47, v251, 12
	s_mov_b32 s0, 0xf800000
	s_mov_b32 s3, 0x42fe0000
	v_lshl_add_u64 v[62:63], s[46:47], 0, v[52:53]
	v_add_co_u32_e32 v62, vcc, 0x500000, v62
	v_readlane_b32 s41, v251, 6
	s_nop 0
	v_addc_co_u32_e32 v63, vcc, 0, v63, vcc
	v_lshl_add_u64 v[130:131], v[62:63], 0, v[54:55]
	global_load_dwordx2 v[64:65], v[62:63], off
	global_load_dwordx2 v[70:71], v[62:63], off offset:512
	global_load_dwordx2 v[76:77], v[62:63], off offset:1024
	s_nop 0
	global_load_dwordx2 v[62:63], v[62:63], off offset:1536
	global_load_dwordx2 v[132:133], v[130:131], off
	global_load_dwordx2 v[132:133], v[130:131], off offset:512
	global_load_dwordx2 v[132:133], v[130:131], off offset:1024
	global_load_dwordx2 v[132:133], v[130:131], off offset:1536
	v_readlane_b32 s42, v251, 7
	v_readlane_b32 s43, v251, 8
	v_readlane_b32 s44, v251, 9
	v_readlane_b32 s45, v251, 10
	s_waitcnt vmcnt(7)
	v_and_b32_e32 v89, 0xffff0000, v65
	v_and_b32_e32 v79, 0xffff0000, v64
	v_lshlrev_b32_e32 v88, 16, v65
	s_waitcnt vmcnt(4)
	v_lshlrev_b32_e32 v75, 16, v62
	v_and_b32_e32 v73, 0xffff0000, v62
	v_mul_f32_e32 v62, v89, v89
	v_lshlrev_b32_e32 v69, 16, v71
	v_lshlrev_b32_e32 v68, 16, v70
	v_and_b32_e32 v71, 0xffff0000, v71
	v_and_b32_e32 v70, 0xffff0000, v70
	v_lshlrev_b32_e32 v80, 16, v63
	v_and_b32_e32 v81, 0xffff0000, v63
	v_lshlrev_b32_e32 v78, 16, v64
	v_pk_fma_f32 v[90:91], v[88:89], v[88:89], v[62:63] op_sel_hi:[1,1,0]
	v_pk_mul_f32 v[62:63], v[70:71], v[70:71]
	v_mul_f32_e32 v72, v79, v79
	v_pk_fma_f32 v[92:93], v[68:69], v[68:69], v[62:63]
	v_lshlrev_b32_e32 v62, 16, v76
	v_and_b32_e32 v63, 0xffff0000, v76
	v_lshlrev_b32_e32 v64, 16, v77
	v_and_b32_e32 v65, 0xffff0000, v77
	v_pk_fma_f32 v[76:77], v[78:79], v[78:79], v[72:73] op_sel_hi:[1,1,0]
	v_mov_b32_e32 v94, v90
	v_mov_b32_e32 v74, v76
	v_mov_b32_e32 v95, v75
	v_pk_add_f32 v[76:77], v[76:77], v[90:91]
	v_pk_mul_f32 v[90:91], v[74:75], v[94:95]
	v_mul_f32_e32 v87, v73, v73
	v_mov_b32_e32 v77, v91
	v_pk_add_f32 v[90:91], v[92:93], v[92:93] op_sel:[0,1] op_sel_hi:[1,0]
	v_mul_f32_e32 v72, v63, v63
	v_mov_b32_e32 v91, v87
	v_pk_add_f32 v[76:77], v[76:77], v[90:91]
	v_pk_fma_f32 v[90:91], v[62:63], v[62:63], v[72:73] op_sel_hi:[1,1,0]
	v_mul_f32_e32 v72, v65, v65
	v_mul_f32_e32 v96, v80, v80
	v_mul_f32_e32 v97, v81, v81
	v_pk_fma_f32 v[92:93], v[64:65], v[64:65], v[72:73] op_sel_hi:[1,1,0]
	v_mov_b32_e32 v91, v96
	v_mov_b32_e32 v93, v97
	v_pk_add_f32 v[90:91], v[90:91], v[92:93]
	s_nop 0
	v_pk_add_f32 v[76:77], v[76:77], v[90:91]
	s_nop 0
	v_add_f32_e32 v72, v76, v77
	ds_bpermute_b32 v74, v1, v72
	s_waitcnt lgkmcnt(0)
	v_add_f32_e32 v72, v72, v74
	ds_bpermute_b32 v74, v82, v72
	s_waitcnt lgkmcnt(0)
	v_add_f32_e32 v72, v72, v74
	ds_bpermute_b32 v74, v83, v72
	s_waitcnt lgkmcnt(0)
	v_add_f32_e32 v72, v72, v74
	ds_bpermute_b32 v74, v84, v72
	s_waitcnt lgkmcnt(0)
	v_add_f32_e32 v72, v72, v74
	ds_bpermute_b32 v74, v85, v72
	s_waitcnt lgkmcnt(0)
	v_add_f32_e32 v72, v72, v74
	ds_bpermute_b32 v74, v86, v72
	s_waitcnt lgkmcnt(0)
	v_add_f32_e32 v72, v72, v74
	v_fmamk_f32 v72, v72, 0x3a800000, v241
	v_cmp_gt_f32_e32 vcc, s0, v72
	v_mul_f32_e32 v74, 0x4f800000, v72
	s_nop 0
	v_cndmask_b32_e32 v72, v72, v74, vcc
	v_sqrt_f32_e32 v74, v72
	s_nop 0
	v_add_u32_e32 v76, -1, v74
	v_fma_f32 v77, -v76, v74, v72
	v_cmp_ge_f32_e64 s[0:1], 0, v77
	v_add_u32_e32 v77, 1, v74
	s_nop 0
	v_cndmask_b32_e64 v76, v74, v76, s[0:1]
	v_fma_f32 v74, -v77, v74, v72
	v_cmp_lt_f32_e64 s[0:1], 0, v74
	s_nop 1
	v_cndmask_b32_e64 v74, v76, v77, s[0:1]
	v_mul_f32_e32 v76, 0x37800000, v74
	v_cndmask_b32_e32 v74, v74, v76, vcc
	v_cmp_class_f32_e32 vcc, v72, v188
	s_nop 1
	v_cndmask_b32_e32 v72, v74, v72, vcc
	v_div_scale_f32 v74, s[0:1], v72, v72, 1.0
	v_rcp_f32_e32 v76, v74
	s_nop 0
	v_fma_f32 v77, -v74, v76, 1.0
	v_fmac_f32_e32 v76, v77, v76
	v_div_scale_f32 v77, vcc, 1.0, v72, 1.0
	v_mul_f32_e32 v87, v77, v76
	v_fma_f32 v90, -v74, v87, v77
	v_fmac_f32_e32 v87, v90, v76
	v_fma_f32 v74, -v74, v87, v77
	v_div_fmas_f32 v74, v74, v76, v87
	v_div_fixup_f32 v74, v74, v72, 1.0
	v_pk_mul_f32 v[76:77], v[74:75], v[88:89] op_sel_hi:[0,1]
	v_pk_mul_f32 v[76:77], v[4:5], v[76:77]
	v_pk_add_f32 v[88:89], v[20:21], 1.0 op_sel_hi:[1,0]
	v_pk_mul_f32 v[78:79], v[74:75], v[78:79] op_sel_hi:[0,1]
	v_pk_fma_f32 v[76:77], v[88:89], v[76:77], v[40:41]
	v_mov_b32_e32 v88, v69
	v_mov_b32_e32 v89, v71
	v_mov_b32_e32 v69, v70
	v_mov_b32_e32 v72, v75
	v_pk_mul_f32 v[78:79], v[2:3], v[78:79]
	v_pk_add_f32 v[90:91], v[18:19], 1.0 op_sel_hi:[1,0]
	v_pk_mul_f32 v[88:89], v[74:75], v[88:89] op_sel_hi:[0,1]
	v_pk_mul_f32 v[68:69], v[74:75], v[68:69] op_sel_hi:[0,1]
	v_pk_mul_f32 v[80:81], v[80:81], v[74:75] op_sel_hi:[1,0]
	v_pk_mul_f32 v[72:73], v[72:73], v[74:75] op_sel_hi:[1,0]
	v_pk_fma_f32 v[78:79], v[90:91], v[78:79], v[38:39]
	v_pk_mul_f32 v[70:71], v[6:7], v[68:69]
	v_pk_mul_f32 v[68:69], v[8:9], v[88:89]
	v_pk_add_f32 v[88:89], v[24:25], 1.0 op_sel_hi:[1,0]
	v_pk_add_f32 v[90:91], v[22:23], 1.0 op_sel_hi:[1,0]
	v_pk_mul_f32 v[64:65], v[74:75], v[64:65] op_sel_hi:[0,1]
	v_pk_mul_f32 v[62:63], v[74:75], v[62:63] op_sel_hi:[0,1]
	v_pk_mul_f32 v[74:75], v[14:15], v[72:73]
	v_pk_mul_f32 v[72:73], v[16:17], v[80:81]
	v_pk_add_f32 v[80:81], v[32:33], 1.0 op_sel_hi:[1,0]
	v_pk_fma_f32 v[68:69], v[88:89], v[68:69], v[28:29]
	v_pk_fma_f32 v[70:71], v[90:91], v[70:71], v[26:27]
	v_pk_mul_f32 v[88:89], v[10:11], v[62:63]
	v_pk_mul_f32 v[62:63], v[12:13], v[64:65]
	v_pk_add_f32 v[64:65], v[36:37], 1.0 op_sel_hi:[1,0]
	v_pk_add_f32 v[90:91], v[34:35], 1.0 op_sel_hi:[1,0]
	v_pk_fma_f32 v[72:73], v[80:81], v[72:73], v[48:49]
	v_max_f32_e64 v80, |v78|, |v79|
	v_max_f32_e64 v81, |v76|, |v77|
	v_pk_fma_f32 v[62:63], v[64:65], v[62:63], v[44:45]
	v_pk_fma_f32 v[64:65], v[90:91], v[88:89], v[42:43]
	v_pk_add_f32 v[88:89], v[30:31], 1.0 op_sel_hi:[1,0]
	v_max3_f32 v80, v80, 0, v81
	v_max_f32_e64 v81, |v70|, |v71|
	v_max_f32_e64 v87, |v68|, |v69|
	v_pk_fma_f32 v[74:75], v[88:89], v[74:75], v[46:47]
	v_max3_f32 v80, v80, v81, v87
	v_max_f32_e64 v81, |v64|, |v65|
	v_max_f32_e64 v87, |v62|, |v63|
	v_max3_f32 v80, v80, v81, v87
	v_max_f32_e64 v81, |v74|, |v75|
	v_max_f32_e64 v87, |v72|, |v73|
	v_max3_f32 v80, v80, v81, v87
	ds_bpermute_b32 v81, v1, v80
	s_waitcnt lgkmcnt(0)
	v_max_f32_e32 v81, v81, v81
	v_max_f32_e32 v80, v80, v81
	ds_bpermute_b32 v81, v82, v80
	s_waitcnt lgkmcnt(0)
	v_max_f32_e32 v81, v81, v81
	v_max_f32_e32 v80, v80, v81
	ds_bpermute_b32 v81, v83, v80
	s_waitcnt lgkmcnt(0)
	v_max_f32_e32 v81, v81, v81
	v_max_f32_e32 v80, v80, v81
	ds_bpermute_b32 v81, v84, v80
	s_waitcnt lgkmcnt(0)
	v_max_f32_e32 v81, v81, v81
	v_max_f32_e32 v80, v80, v81
	ds_bpermute_b32 v81, v85, v80
	s_waitcnt lgkmcnt(0)
	v_max_f32_e32 v81, v81, v81
	v_max_f32_e32 v80, v80, v81
	ds_bpermute_b32 v81, v86, v80
	s_waitcnt lgkmcnt(0)
	v_max_f32_e32 v81, v81, v81
	v_max_f32_e32 v80, v80, v81
	v_div_scale_f32 v81, s[10:11], v80, v80, s3
	v_rcp_f32_e32 v87, v81
	v_cmp_lt_f32_e64 s[0:1], 0, v80
	v_fma_f32 v88, -v81, v87, 1.0
	v_fmac_f32_e32 v87, v88, v87
	v_div_scale_f32 v88, vcc, s3, v80, s3
	v_mul_f32_e32 v89, v88, v87
	v_fma_f32 v90, -v81, v89, v88
	v_fmac_f32_e32 v89, v90, v87
	v_fma_f32 v81, -v81, v89, v88
	v_div_fmas_f32 v81, v81, v87, v89
	v_div_fixup_f32 v81, v81, v80, s3
	v_cndmask_b32_e64 v81, 0, v81, s[0:1]
	v_mul_f32_e32 v79, v79, v81
	v_mul_f32_e32 v78, v78, v81
	v_rndne_f32_e32 v79, v79
	v_mul_f32_e32 v76, v76, v81
	v_mul_f32_e32 v77, v77, v81
	v_mul_f32_e32 v65, v65, v81
	v_rndne_f32_e32 v78, v78
	v_cvt_i32_f32_e32 v79, v79
	v_rndne_f32_e32 v76, v76
	v_rndne_f32_e32 v77, v77
	v_mul_f32_e32 v64, v64, v81
	v_rndne_f32_e32 v65, v65
	v_mul_f32_e32 v62, v62, v81
	v_mul_f32_e32 v63, v63, v81
	v_cvt_i32_f32_e32 v78, v78
	v_cvt_i32_f32_sdwa v76, v76 dst_sel:WORD_1 dst_unused:UNUSED_PAD src0_sel:DWORD
	v_cvt_i32_f32_e32 v77, v77
	v_rndne_f32_e32 v64, v64
	v_cvt_i32_f32_e32 v65, v65
	v_rndne_f32_e32 v62, v62
	v_rndne_f32_e32 v63, v63
	v_cvt_i32_f32_e32 v64, v64
	v_cvt_i32_f32_sdwa v62, v62 dst_sel:WORD_1 dst_unused:UNUSED_PAD src0_sel:DWORD
	v_cvt_i32_f32_e32 v63, v63
	v_lshlrev_b32_e32 v79, 8, v79
	s_mov_b32 s0, 0x40c0c00
	v_lshl_add_u64 v[88:89], s[46:47], 0, v[56:57]
	v_and_b32_e32 v79, 0xff00, v79
	v_and_b32_e32 v76, 0xff0000, v76
	v_perm_b32 v77, v77, v78, s0
	s_mov_b32 s1, 0x8900000
	v_lshlrev_b32_e32 v65, 8, v65
	v_or3_b32 v78, v77, v79, v76
	v_add_co_u32_e32 v76, vcc, s1, v88
	v_and_b32_e32 v65, 0xff00, v65
	v_and_b32_e32 v62, 0xff0000, v62
	v_perm_b32 v63, v63, v64, s0
	v_addc_co_u32_e32 v77, vcc, 0, v89, vcc
	v_mul_f32_e32 v71, v71, v81
	v_or3_b32 v62, v63, v65, v62
	v_mul_f32_e32 v63, v75, v81
	v_mul_f32_e32 v70, v70, v81
	v_rndne_f32_e32 v71, v71
	v_mul_f32_e32 v68, v68, v81
	v_mul_f32_e32 v69, v69, v81
	global_store_dword v[76:77], v62, off offset:512
	v_mul_f32_e32 v62, v74, v81
	v_rndne_f32_e32 v63, v63
	v_mul_f32_e32 v64, v72, v81
	v_mul_f32_e32 v65, v73, v81
	v_rndne_f32_e32 v70, v70
	v_cvt_i32_f32_e32 v71, v71
	v_rndne_f32_e32 v68, v68
	v_rndne_f32_e32 v69, v69
	v_rndne_f32_e32 v62, v62
	v_cvt_i32_f32_e32 v63, v63
	v_rndne_f32_e32 v64, v64
	v_rndne_f32_e32 v65, v65
	v_cvt_i32_f32_e32 v70, v70
	v_cvt_i32_f32_sdwa v68, v68 dst_sel:WORD_1 dst_unused:UNUSED_PAD src0_sel:DWORD
	v_cvt_i32_f32_e32 v69, v69
	v_cvt_i32_f32_e32 v62, v62
	v_cvt_i32_f32_sdwa v64, v64 dst_sel:WORD_1 dst_unused:UNUSED_PAD src0_sel:DWORD
	v_cvt_i32_f32_e32 v65, v65
	v_lshlrev_b32_e32 v71, 8, v71
	v_lshlrev_b32_e32 v63, 8, v63
	v_and_b32_e32 v71, 0xff00, v71
	v_and_b32_e32 v68, 0xff0000, v68
	v_perm_b32 v69, v69, v70, s0
	v_and_b32_e32 v63, 0xff00, v63
	v_and_b32_e32 v64, 0xff0000, v64
	v_perm_b32 v62, v65, v62, s0
	v_or3_b32 v68, v69, v71, v68
	v_or3_b32 v62, v62, v63, v64
	global_store_dword v[76:77], v78, off
	global_store_dword v[76:77], v68, off offset:256
	global_store_dword v[76:77], v62, off offset:768
	s_and_saveexec_b64 s[0:1], s[36:37]
	s_cbranch_execz .LBB0_1627
	v_readlane_b32 s40, v251, 5
	v_readlane_b32 s46, v251, 11
	v_readlane_b32 s47, v251, 12
	v_mul_f32_e32 v64, 0x3c010204, v80
	v_readlane_b32 s41, v251, 6
	v_lshl_add_u64 v[62:63], s[46:47], 0, v[60:61]
	v_readlane_b32 s42, v251, 7
	v_readlane_b32 s43, v251, 8
	v_readlane_b32 s44, v251, 9
	v_readlane_b32 s45, v251, 10
	global_store_dword v[62:63], v64, off
	s_branch .LBB0_1627
